# v38 + top-4 argmax shuffles (xor 8/4/2/1) in P6 via DPP movs instead of ds_bpermute
# baseline (speedup 1.0000x reference)
; __device__ __forceinline__ void p6_router(Frame& F) {
;     ...
;     for (int i = tid; i < 1024; i += 512) { float s = F.in[I_BR][i & 31];
; #pragma unroll
;         for (int w = 0; w < 8; ++w) s += red[w * 1024 + i];
;         lg[i] = s; }
;     __syncthreads();
;     for (int pass = 0; pass < 2; ++pass) {
;         const int row = pass * 16 + (tid >> 5), e = tid & 31;
;         float v = lg[row * 32 + e]; float tl[4]; int te[4];
; #pragma unroll
;         for (int k = 0; k < 4; ++k) {
;             float bv = v; int bi = e;
; #pragma unroll
;             for (int o = 16; o >= 1; o >>= 1) { const float ov = __shfl_xor(bv, o); const int oi = __shfl_xor(bi, o); if (ov > bv || (ov == bv && oi < bi)) { bv = ov; bi = oi; } }
.LBB0_759:
	ds_read2st64_b32 v[6:7], v4 offset1:16
	ds_read2st64_b32 v[8:9], v4 offset0:32 offset1:48
	ds_read2st64_b32 v[10:11], v4 offset0:64 offset1:80
	ds_read2st64_b32 v[12:13], v4 offset0:96 offset1:112
	v_add_co_u32_e32 v3, vcc, 0x200, v3
	s_waitcnt vmcnt(0) lgkmcnt(3)
	v_add_f32_e32 v6, v2, v6
	v_add_f32_e32 v6, v6, v7
	s_waitcnt lgkmcnt(2)
	v_add_f32_e32 v6, v6, v8
	v_add_f32_e32 v6, v6, v9
	s_waitcnt lgkmcnt(1)
	v_add_f32_e32 v6, v6, v10
	v_add_f32_e32 v6, v6, v11
	s_waitcnt lgkmcnt(0)
	v_add_f32_e32 v6, v6, v12
	s_xor_b64 s[4:5], vcc, -1
	v_add_f32_e32 v6, v6, v13
	s_and_b64 s[4:5], exec, s[4:5]
	ds_write_b32 v4, v6 offset:32768
	s_or_b64 s[0:1], s[4:5], s[0:1]
	v_add_u32_e32 v4, 0x800, v4
	s_andn2_b64 exec, exec, s[0:1]
	s_cbranch_execnz .LBB0_759
	s_or_b64 exec, exec, s[0:1]
	v_lshrrev_b32_e32 v2, 5, v0
	v_lshl_add_u32 v3, v5, 2, 0
	v_lshl_add_u32 v4, v2, 7, v3
	s_waitcnt lgkmcnt(0)
	s_barrier
	ds_read_b32 v7, v4 offset:32768
	ds_bpermute_b32 v10, v145, v5
	s_waitcnt lgkmcnt(1)
	ds_bpermute_b32 v9, v145, v7
	v_mov_b32_e32 v4, v7
	s_waitcnt lgkmcnt(0)
	v_cmp_lt_f32_e64 s[4:5], v7, v9
	v_cmp_nlt_f32_e32 vcc, v7, v9
	s_and_saveexec_b64 s[8:9], vcc
	v_cmp_eq_f32_e32 vcc, v7, v9
	v_cmp_lt_i32_e64 s[0:1], v10, v5
	s_and_b64 s[0:1], vcc, s[0:1]
	s_andn2_b64 s[4:5], s[4:5], exec
	s_and_b64 s[0:1], s[0:1], exec
	s_or_b64 s[4:5], s[4:5], s[0:1]
	s_or_b64 exec, exec, s[8:9]
	v_mov_b32_e32 v8, v7
	v_mov_b32_e32 v6, v5
	s_and_saveexec_b64 s[0:1], s[4:5]
	v_mov_b32_e32 v8, v9
	v_mov_b32_e32 v6, v10
	v_mov_b32_e32 v4, v9
	s_or_b64 exec, exec, s[0:1]
	s_nop 1
	v_mov_b32_dpp v9, v8 row_ror:8 row_mask:0xf bank_mask:0xf
	s_nop 1
	v_mov_b32_dpp v10, v6 row_ror:8 row_mask:0xf bank_mask:0xf
	s_waitcnt lgkmcnt(1)
	v_cmp_lt_f32_e64 s[4:5], v4, v9
	v_cmp_nlt_f32_e32 vcc, v4, v9
	s_and_saveexec_b64 s[8:9], vcc
	s_cbranch_execz .LBB0_766
	v_cmp_eq_f32_e32 vcc, v4, v9
	s_waitcnt lgkmcnt(0)
	v_cmp_lt_i32_e64 s[0:1], v10, v6
	s_and_b64 s[0:1], vcc, s[0:1]
	s_andn2_b64 s[4:5], s[4:5], exec
	s_and_b64 s[0:1], s[0:1], exec
	s_or_b64 s[4:5], s[4:5], s[0:1]

; __device__ __forceinline__ void p6_router(Frame& F) {
;     ...
;             for (int o = 16; o >= 1; o >>= 1) { const float ov = __shfl_xor(bv, o); const int oi = __shfl_xor(bi, o); if (ov > bv || (ov == bv && oi < bi)) { bv = ov; bi = oi; } }
.LBB0_768:
	s_or_b64 exec, exec, s[0:1]
	s_nop 1
	v_mov_b32_dpp v9, v8 row_shl:4 row_mask:0xf bank_mask:0x5
	s_nop 1
	v_mov_b32_dpp v9, v8 row_shr:4 row_mask:0xf bank_mask:0xa
	s_waitcnt lgkmcnt(1)
	s_nop 1
	v_mov_b32_dpp v10, v6 row_shl:4 row_mask:0xf bank_mask:0x5
	s_nop 1
	v_mov_b32_dpp v10, v6 row_shr:4 row_mask:0xf bank_mask:0xa
	s_waitcnt lgkmcnt(1)
	v_cmp_lt_f32_e64 s[4:5], v4, v9
	v_cmp_nlt_f32_e32 vcc, v4, v9
	s_and_saveexec_b64 s[8:9], vcc
	s_cbranch_execz .LBB0_770
	v_cmp_eq_f32_e32 vcc, v4, v9
	s_waitcnt lgkmcnt(0)
	v_cmp_lt_i32_e64 s[0:1], v10, v6
	s_and_b64 s[0:1], vcc, s[0:1]
	s_andn2_b64 s[4:5], s[4:5], exec
	s_and_b64 s[0:1], s[0:1], exec
	s_or_b64 s[4:5], s[4:5], s[0:1]

; __device__ __forceinline__ void p6_router(Frame& F) {
;     ...
;             for (int o = 16; o >= 1; o >>= 1) { const float ov = __shfl_xor(bv, o); const int oi = __shfl_xor(bi, o); if (ov > bv || (ov == bv && oi < bi)) { bv = ov; bi = oi; } }
.LBB0_772:
	s_or_b64 exec, exec, s[0:1]
	s_nop 1
	v_mov_b32_dpp v9, v8 quad_perm:[2,3,0,1] row_mask:0xf bank_mask:0xf
	s_waitcnt lgkmcnt(1)
	s_nop 1
	v_mov_b32_dpp v10, v6 quad_perm:[2,3,0,1] row_mask:0xf bank_mask:0xf
	s_waitcnt lgkmcnt(1)
	v_cmp_lt_f32_e64 s[4:5], v4, v9
	v_cmp_nlt_f32_e32 vcc, v4, v9
	s_and_saveexec_b64 s[8:9], vcc
	s_cbranch_execz .LBB0_774
	v_cmp_eq_f32_e32 vcc, v4, v9
	s_waitcnt lgkmcnt(0)
	v_cmp_lt_i32_e64 s[0:1], v10, v6
	s_and_b64 s[0:1], vcc, s[0:1]
	s_andn2_b64 s[4:5], s[4:5], exec
	s_and_b64 s[0:1], s[0:1], exec
	s_or_b64 s[4:5], s[4:5], s[0:1]

; __device__ __forceinline__ void p6_router(Frame& F) {
;     ...
;             for (int o = 16; o >= 1; o >>= 1) { const float ov = __shfl_xor(bv, o); const int oi = __shfl_xor(bi, o); if (ov > bv || (ov == bv && oi < bi)) { bv = ov; bi = oi; } }
.LBB0_776:
	s_or_b64 exec, exec, s[0:1]
	s_nop 1
	v_mov_b32_dpp v8, v8 quad_perm:[1,0,3,2] row_mask:0xf bank_mask:0xf
	s_nop 1
	v_mov_b32_dpp v9, v6 quad_perm:[1,0,3,2] row_mask:0xf bank_mask:0xf
	s_waitcnt lgkmcnt(1)
	v_cmp_lt_f32_e64 s[4:5], v4, v8
	v_cmp_nlt_f32_e32 vcc, v4, v8
	s_and_saveexec_b64 s[8:9], vcc
	s_cbranch_execz .LBB0_778
	v_cmp_eq_f32_e32 vcc, v4, v8
	s_waitcnt lgkmcnt(0)
	v_cmp_lt_i32_e64 s[0:1], v9, v6
	s_and_b64 s[0:1], vcc, s[0:1]
	s_andn2_b64 s[4:5], s[4:5], exec
	s_and_b64 s[0:1], s[0:1], exec
	s_or_b64 s[4:5], s[4:5], s[0:1]

; __device__ __forceinline__ void p6_router(Frame& F) {
;     ...
;             float bv = v; int bi = e;
; #pragma unroll
;             for (int o = 16; o >= 1; o >>= 1) { const float ov = __shfl_xor(bv, o); const int oi = __shfl_xor(bi, o); if (ov > bv || (ov == bv && oi < bi)) { bv = ov; bi = oi; } }
;             tl[k] = bv; te[k] = bi; if (e == bi) v = -INFINITY;
.LBB0_780:
	s_or_b64 exec, exec, s[0:1]
	v_mov_b32_e32 v8, 0xff800000
	v_cmp_ne_u32_e32 vcc, v5, v6
	ds_bpermute_b32 v12, v145, v5
	s_nop 0
	v_cndmask_b32_e32 v8, v8, v7, vcc
	ds_bpermute_b32 v11, v145, v8
	s_waitcnt lgkmcnt(0)
	v_cmp_lt_f32_e64 s[4:5], v8, v11
	v_cmp_nlt_f32_e32 vcc, v8, v11
	s_and_saveexec_b64 s[8:9], vcc
	v_cmp_eq_f32_e32 vcc, v8, v11
	v_cmp_lt_i32_e64 s[0:1], v12, v5
	s_and_b64 s[0:1], vcc, s[0:1]
	s_andn2_b64 s[4:5], s[4:5], exec
	s_and_b64 s[0:1], s[0:1], exec
	s_or_b64 s[4:5], s[4:5], s[0:1]
	s_or_b64 exec, exec, s[8:9]
	v_mov_b32_e32 v9, v8
	v_mov_b32_e32 v7, v5
	v_mov_b32_e32 v10, v8
	s_and_saveexec_b64 s[0:1], s[4:5]
	v_mov_b32_e32 v9, v11
	v_mov_b32_e32 v7, v12
	v_mov_b32_e32 v10, v11
	s_or_b64 exec, exec, s[0:1]
	s_nop 1
	v_mov_b32_dpp v11, v9 row_ror:8 row_mask:0xf bank_mask:0xf
	s_nop 1
	v_mov_b32_dpp v12, v7 row_ror:8 row_mask:0xf bank_mask:0xf
	s_waitcnt lgkmcnt(1)
	v_cmp_lt_f32_e64 s[4:5], v10, v11
	v_cmp_nlt_f32_e32 vcc, v10, v11
	s_and_saveexec_b64 s[8:9], vcc
	s_cbranch_execz .LBB0_786
	v_cmp_eq_f32_e32 vcc, v10, v11
	s_waitcnt lgkmcnt(0)
	v_cmp_lt_i32_e64 s[0:1], v12, v7
	s_and_b64 s[0:1], vcc, s[0:1]
	s_andn2_b64 s[4:5], s[4:5], exec
	s_and_b64 s[0:1], s[0:1], exec
	s_or_b64 s[4:5], s[4:5], s[0:1]

; __device__ __forceinline__ void p6_router(Frame& F) {
;     ...
;             for (int o = 16; o >= 1; o >>= 1) { const float ov = __shfl_xor(bv, o); const int oi = __shfl_xor(bi, o); if (ov > bv || (ov == bv && oi < bi)) { bv = ov; bi = oi; } }
.LBB0_788:
	s_or_b64 exec, exec, s[0:1]
	s_nop 1
	v_mov_b32_dpp v11, v9 row_shl:4 row_mask:0xf bank_mask:0x5
	s_nop 1
	v_mov_b32_dpp v11, v9 row_shr:4 row_mask:0xf bank_mask:0xa
	s_waitcnt lgkmcnt(1)
	s_nop 1
	v_mov_b32_dpp v12, v7 row_shl:4 row_mask:0xf bank_mask:0x5
	s_nop 1
	v_mov_b32_dpp v12, v7 row_shr:4 row_mask:0xf bank_mask:0xa
	s_waitcnt lgkmcnt(1)
	v_cmp_lt_f32_e64 s[4:5], v10, v11
	v_cmp_nlt_f32_e32 vcc, v10, v11
	s_and_saveexec_b64 s[8:9], vcc
	s_cbranch_execz .LBB0_790
	v_cmp_eq_f32_e32 vcc, v10, v11
	s_waitcnt lgkmcnt(0)
	v_cmp_lt_i32_e64 s[0:1], v12, v7
	s_and_b64 s[0:1], vcc, s[0:1]
	s_andn2_b64 s[4:5], s[4:5], exec
	s_and_b64 s[0:1], s[0:1], exec
	s_or_b64 s[4:5], s[4:5], s[0:1]

; __device__ __forceinline__ void p6_router(Frame& F) {
;     ...
;             for (int o = 16; o >= 1; o >>= 1) { const float ov = __shfl_xor(bv, o); const int oi = __shfl_xor(bi, o); if (ov > bv || (ov == bv && oi < bi)) { bv = ov; bi = oi; } }
.LBB0_792:
	s_or_b64 exec, exec, s[0:1]
	s_nop 1
	v_mov_b32_dpp v11, v9 quad_perm:[2,3,0,1] row_mask:0xf bank_mask:0xf
	s_waitcnt lgkmcnt(1)
	s_nop 1
	v_mov_b32_dpp v12, v7 quad_perm:[2,3,0,1] row_mask:0xf bank_mask:0xf
	s_waitcnt lgkmcnt(1)
	v_cmp_lt_f32_e64 s[4:5], v10, v11
	v_cmp_nlt_f32_e32 vcc, v10, v11
	s_and_saveexec_b64 s[8:9], vcc
	s_cbranch_execz .LBB0_794
	v_cmp_eq_f32_e32 vcc, v10, v11
	s_waitcnt lgkmcnt(0)
	v_cmp_lt_i32_e64 s[0:1], v12, v7
	s_and_b64 s[0:1], vcc, s[0:1]
	s_andn2_b64 s[4:5], s[4:5], exec
	s_and_b64 s[0:1], s[0:1], exec
	s_or_b64 s[4:5], s[4:5], s[0:1]

; __device__ __forceinline__ void p6_router(Frame& F) {
;     ...
;             for (int o = 16; o >= 1; o >>= 1) { const float ov = __shfl_xor(bv, o); const int oi = __shfl_xor(bi, o); if (ov > bv || (ov == bv && oi < bi)) { bv = ov; bi = oi; } }
.LBB0_796:
	s_or_b64 exec, exec, s[0:1]
	s_nop 1
	v_mov_b32_dpp v9, v9 quad_perm:[1,0,3,2] row_mask:0xf bank_mask:0xf
	s_nop 1
	v_mov_b32_dpp v11, v7 quad_perm:[1,0,3,2] row_mask:0xf bank_mask:0xf
	s_waitcnt lgkmcnt(1)
	v_cmp_lt_f32_e64 s[4:5], v10, v9
	v_cmp_nlt_f32_e32 vcc, v10, v9
	s_and_saveexec_b64 s[8:9], vcc
	s_cbranch_execz .LBB0_798
	v_cmp_eq_f32_e32 vcc, v10, v9
	s_waitcnt lgkmcnt(0)
	v_cmp_lt_i32_e64 s[0:1], v11, v7
	s_and_b64 s[0:1], vcc, s[0:1]
	s_andn2_b64 s[4:5], s[4:5], exec
	s_and_b64 s[0:1], s[0:1], exec
	s_or_b64 s[4:5], s[4:5], s[0:1]

; __device__ __forceinline__ void p6_router(Frame& F) {
;     ...
;             float bv = v; int bi = e;
; #pragma unroll
;             for (int o = 16; o >= 1; o >>= 1) { const float ov = __shfl_xor(bv, o); const int oi = __shfl_xor(bi, o); if (ov > bv || (ov == bv && oi < bi)) { bv = ov; bi = oi; } }
;             tl[k] = bv; te[k] = bi; if (e == bi) v = -INFINITY;
.LBB0_800:
	s_or_b64 exec, exec, s[0:1]
	v_mov_b32_e32 v9, 0xff800000
	v_cmp_ne_u32_e32 vcc, v5, v7
	ds_bpermute_b32 v14, v145, v5
	s_nop 0
	v_cndmask_b32_e32 v9, v9, v8, vcc
	ds_bpermute_b32 v13, v145, v9
	s_waitcnt lgkmcnt(0)
	v_cmp_lt_f32_e64 s[4:5], v9, v13
	v_cmp_nlt_f32_e32 vcc, v9, v13
	s_and_saveexec_b64 s[8:9], vcc
	v_cmp_eq_f32_e32 vcc, v9, v13
	v_cmp_lt_i32_e64 s[0:1], v14, v5
	s_and_b64 s[0:1], vcc, s[0:1]
	s_andn2_b64 s[4:5], s[4:5], exec
	s_and_b64 s[0:1], s[0:1], exec
	s_or_b64 s[4:5], s[4:5], s[0:1]
	s_or_b64 exec, exec, s[8:9]
	v_mov_b32_e32 v12, v9
	v_mov_b32_e32 v8, v5
	v_mov_b32_e32 v11, v9
	s_and_saveexec_b64 s[0:1], s[4:5]
	v_mov_b32_e32 v12, v13
	v_mov_b32_e32 v8, v14
	v_mov_b32_e32 v11, v13
	s_or_b64 exec, exec, s[0:1]
	s_nop 1
	v_mov_b32_dpp v13, v12 row_ror:8 row_mask:0xf bank_mask:0xf
	s_nop 1
	v_mov_b32_dpp v14, v8 row_ror:8 row_mask:0xf bank_mask:0xf
	s_waitcnt lgkmcnt(1)
	v_cmp_lt_f32_e64 s[4:5], v11, v13
	v_cmp_nlt_f32_e32 vcc, v11, v13
	s_and_saveexec_b64 s[8:9], vcc
	s_cbranch_execz .LBB0_806
	v_cmp_eq_f32_e32 vcc, v11, v13
	s_waitcnt lgkmcnt(0)
	v_cmp_lt_i32_e64 s[0:1], v14, v8
	s_and_b64 s[0:1], vcc, s[0:1]
	s_andn2_b64 s[4:5], s[4:5], exec
	s_and_b64 s[0:1], s[0:1], exec
	s_or_b64 s[4:5], s[4:5], s[0:1]

; __device__ __forceinline__ void p6_router(Frame& F) {
;     ...
;             for (int o = 16; o >= 1; o >>= 1) { const float ov = __shfl_xor(bv, o); const int oi = __shfl_xor(bi, o); if (ov > bv || (ov == bv && oi < bi)) { bv = ov; bi = oi; } }
.LBB0_808:
	s_or_b64 exec, exec, s[0:1]
	s_nop 1
	v_mov_b32_dpp v13, v12 row_shl:4 row_mask:0xf bank_mask:0x5
	s_nop 1
	v_mov_b32_dpp v13, v12 row_shr:4 row_mask:0xf bank_mask:0xa
	s_waitcnt lgkmcnt(1)
	s_nop 1
	v_mov_b32_dpp v14, v8 row_shl:4 row_mask:0xf bank_mask:0x5
	s_nop 1
	v_mov_b32_dpp v14, v8 row_shr:4 row_mask:0xf bank_mask:0xa
	s_waitcnt lgkmcnt(1)
	v_cmp_lt_f32_e64 s[4:5], v11, v13
	v_cmp_nlt_f32_e32 vcc, v11, v13
	s_and_saveexec_b64 s[8:9], vcc
	s_cbranch_execz .LBB0_810
	v_cmp_eq_f32_e32 vcc, v11, v13
	s_waitcnt lgkmcnt(0)
	v_cmp_lt_i32_e64 s[0:1], v14, v8
	s_and_b64 s[0:1], vcc, s[0:1]
	s_andn2_b64 s[4:5], s[4:5], exec
	s_and_b64 s[0:1], s[0:1], exec
	s_or_b64 s[4:5], s[4:5], s[0:1]

; __device__ __forceinline__ void p6_router(Frame& F) {
;     ...
;             for (int o = 16; o >= 1; o >>= 1) { const float ov = __shfl_xor(bv, o); const int oi = __shfl_xor(bi, o); if (ov > bv || (ov == bv && oi < bi)) { bv = ov; bi = oi; } }
.LBB0_812:
	s_or_b64 exec, exec, s[0:1]
	s_nop 1
	v_mov_b32_dpp v13, v12 quad_perm:[2,3,0,1] row_mask:0xf bank_mask:0xf
	s_waitcnt lgkmcnt(1)
	s_nop 1
	v_mov_b32_dpp v14, v8 quad_perm:[2,3,0,1] row_mask:0xf bank_mask:0xf
	s_waitcnt lgkmcnt(1)
	v_cmp_lt_f32_e64 s[4:5], v11, v13
	v_cmp_nlt_f32_e32 vcc, v11, v13
	s_and_saveexec_b64 s[8:9], vcc
	s_cbranch_execz .LBB0_814
	v_cmp_eq_f32_e32 vcc, v11, v13
	s_waitcnt lgkmcnt(0)
	v_cmp_lt_i32_e64 s[0:1], v14, v8
	s_and_b64 s[0:1], vcc, s[0:1]
	s_andn2_b64 s[4:5], s[4:5], exec
	s_and_b64 s[0:1], s[0:1], exec
	s_or_b64 s[4:5], s[4:5], s[0:1]

; __device__ __forceinline__ void p6_router(Frame& F) {
;     ...
;             for (int o = 16; o >= 1; o >>= 1) { const float ov = __shfl_xor(bv, o); const int oi = __shfl_xor(bi, o); if (ov > bv || (ov == bv && oi < bi)) { bv = ov; bi = oi; } }
.LBB0_816:
	s_or_b64 exec, exec, s[0:1]
	s_nop 1
	v_mov_b32_dpp v12, v12 quad_perm:[1,0,3,2] row_mask:0xf bank_mask:0xf
	s_nop 1
	v_mov_b32_dpp v13, v8 quad_perm:[1,0,3,2] row_mask:0xf bank_mask:0xf
	s_waitcnt lgkmcnt(1)
	v_cmp_lt_f32_e64 s[4:5], v11, v12
	v_cmp_nlt_f32_e32 vcc, v11, v12
	s_and_saveexec_b64 s[8:9], vcc
	s_cbranch_execz .LBB0_818
	v_cmp_eq_f32_e32 vcc, v11, v12
	s_waitcnt lgkmcnt(0)
	v_cmp_lt_i32_e64 s[0:1], v13, v8
	s_and_b64 s[0:1], vcc, s[0:1]
	s_andn2_b64 s[4:5], s[4:5], exec
	s_and_b64 s[0:1], s[0:1], exec
	s_or_b64 s[4:5], s[4:5], s[0:1]

; __device__ __forceinline__ void p6_router(Frame& F) {
;     ...
;             float bv = v; int bi = e;
; #pragma unroll
;             for (int o = 16; o >= 1; o >>= 1) { const float ov = __shfl_xor(bv, o); const int oi = __shfl_xor(bi, o); if (ov > bv || (ov == bv && oi < bi)) { bv = ov; bi = oi; } }
;             tl[k] = bv; te[k] = bi; if (e == bi) v = -INFINITY;
.LBB0_820:
	s_or_b64 exec, exec, s[0:1]
	v_mov_b32_e32 v12, 0xff800000
	v_cmp_ne_u32_e32 vcc, v5, v8
	ds_bpermute_b32 v14, v145, v5
	s_nop 0
	v_cndmask_b32_e32 v12, v12, v9, vcc
	s_waitcnt lgkmcnt(1)
	ds_bpermute_b32 v13, v145, v12
	s_waitcnt lgkmcnt(0)
	v_cmp_lt_f32_e64 s[4:5], v12, v13
	v_cmp_nlt_f32_e32 vcc, v12, v13
	s_and_saveexec_b64 s[8:9], vcc
	v_cmp_eq_f32_e32 vcc, v12, v13
	v_cmp_lt_i32_e64 s[0:1], v14, v5
	s_and_b64 s[0:1], vcc, s[0:1]
	s_andn2_b64 s[4:5], s[4:5], exec
	s_and_b64 s[0:1], s[0:1], exec
	s_or_b64 s[4:5], s[4:5], s[0:1]
	s_or_b64 exec, exec, s[8:9]
	v_mov_b32_e32 v9, v5
	s_and_saveexec_b64 s[0:1], s[4:5]
	v_mov_b32_e32 v12, v13
	v_mov_b32_e32 v9, v14
	s_or_b64 exec, exec, s[0:1]
	s_nop 1
	v_mov_b32_dpp v13, v12 row_ror:8 row_mask:0xf bank_mask:0xf
	s_nop 1
	v_mov_b32_dpp v14, v9 row_ror:8 row_mask:0xf bank_mask:0xf
	s_waitcnt lgkmcnt(1)
	v_cmp_lt_f32_e64 s[4:5], v12, v13
	v_cmp_nlt_f32_e32 vcc, v12, v13
	s_and_saveexec_b64 s[8:9], vcc
	s_cbranch_execz .LBB0_826
	v_cmp_eq_f32_e32 vcc, v12, v13
	s_waitcnt lgkmcnt(0)
	v_cmp_lt_i32_e64 s[0:1], v14, v9
	s_and_b64 s[0:1], vcc, s[0:1]
	s_andn2_b64 s[4:5], s[4:5], exec
	s_and_b64 s[0:1], s[0:1], exec
	s_or_b64 s[4:5], s[4:5], s[0:1]

; __device__ __forceinline__ void p6_router(Frame& F) {
;     ...
;             for (int o = 16; o >= 1; o >>= 1) { const float ov = __shfl_xor(bv, o); const int oi = __shfl_xor(bi, o); if (ov > bv || (ov == bv && oi < bi)) { bv = ov; bi = oi; } }
.LBB0_828:
	s_or_b64 exec, exec, s[0:1]
	s_nop 1
	v_mov_b32_dpp v13, v12 row_shl:4 row_mask:0xf bank_mask:0x5
	s_nop 1
	v_mov_b32_dpp v13, v12 row_shr:4 row_mask:0xf bank_mask:0xa
	s_waitcnt lgkmcnt(1)
	s_nop 1
	v_mov_b32_dpp v14, v9 row_shl:4 row_mask:0xf bank_mask:0x5
	s_nop 1
	v_mov_b32_dpp v14, v9 row_shr:4 row_mask:0xf bank_mask:0xa
	s_waitcnt lgkmcnt(1)
	v_cmp_lt_f32_e64 s[4:5], v12, v13
	v_cmp_nlt_f32_e32 vcc, v12, v13
	s_and_saveexec_b64 s[8:9], vcc
	s_cbranch_execz .LBB0_830
	v_cmp_eq_f32_e32 vcc, v12, v13
	s_waitcnt lgkmcnt(0)
	v_cmp_lt_i32_e64 s[0:1], v14, v9
	s_and_b64 s[0:1], vcc, s[0:1]
	s_andn2_b64 s[4:5], s[4:5], exec
	s_and_b64 s[0:1], s[0:1], exec
	s_or_b64 s[4:5], s[4:5], s[0:1]

; __device__ __forceinline__ void p6_router(Frame& F) {
;     ...
;             for (int o = 16; o >= 1; o >>= 1) { const float ov = __shfl_xor(bv, o); const int oi = __shfl_xor(bi, o); if (ov > bv || (ov == bv && oi < bi)) { bv = ov; bi = oi; } }
.LBB0_832:
	s_or_b64 exec, exec, s[0:1]
	s_nop 1
	v_mov_b32_dpp v13, v12 quad_perm:[2,3,0,1] row_mask:0xf bank_mask:0xf
	s_waitcnt lgkmcnt(1)
	s_nop 1
	v_mov_b32_dpp v14, v9 quad_perm:[2,3,0,1] row_mask:0xf bank_mask:0xf
	s_waitcnt lgkmcnt(1)
	v_cmp_lt_f32_e64 s[4:5], v12, v13
	v_cmp_nlt_f32_e32 vcc, v12, v13
	s_and_saveexec_b64 s[8:9], vcc
	s_cbranch_execz .LBB0_834
	v_cmp_eq_f32_e32 vcc, v12, v13
	s_waitcnt lgkmcnt(0)
	v_cmp_lt_i32_e64 s[0:1], v14, v9
	s_and_b64 s[0:1], vcc, s[0:1]
	s_andn2_b64 s[4:5], s[4:5], exec
	s_and_b64 s[0:1], s[0:1], exec
	s_or_b64 s[4:5], s[4:5], s[0:1]

; __device__ __forceinline__ void p6_router(Frame& F) {
;     ...
;             for (int o = 16; o >= 1; o >>= 1) { const float ov = __shfl_xor(bv, o); const int oi = __shfl_xor(bi, o); if (ov > bv || (ov == bv && oi < bi)) { bv = ov; bi = oi; } }
;             tl[k] = bv; te[k] = bi; if (e == bi) v = -INFINITY;
.LBB0_836:
	s_or_b64 exec, exec, s[0:1]
	s_nop 1
	v_mov_b32_dpp v13, v12 quad_perm:[1,0,3,2] row_mask:0xf bank_mask:0xf
	s_waitcnt lgkmcnt(1)
	s_nop 1
	v_mov_b32_dpp v14, v9 quad_perm:[1,0,3,2] row_mask:0xf bank_mask:0xf
	s_waitcnt lgkmcnt(1)
	v_cmp_lt_f32_e64 s[4:5], v12, v13
	v_cmp_nlt_f32_e32 vcc, v12, v13
	s_and_saveexec_b64 s[8:9], vcc
	s_cbranch_execz .LBB0_943
	v_cmp_eq_f32_e32 vcc, v12, v13
	s_waitcnt lgkmcnt(0)
	v_cmp_lt_i32_e64 s[0:1], v14, v9
	s_and_b64 s[0:1], vcc, s[0:1]
	s_andn2_b64 s[4:5], s[4:5], exec
	s_and_b64 s[0:1], s[0:1], exec
	s_or_b64 s[4:5], s[4:5], s[0:1]
	s_or_b64 exec, exec, s[8:9]
	s_and_saveexec_b64 s[0:1], s[4:5]
	s_cbranch_execnz .LBB0_944

; __device__ __forceinline__ void p6_router(Frame& F) {
;     ...
;     for (int pass = 0; pass < 2; ++pass) {
;         const int row = pass * 16 + (tid >> 5), e = tid & 31;
;         float v = lg[row * 32 + e]; float tl[4]; int te[4];
; #pragma unroll
;         for (int k = 0; k < 4; ++k) {
;             float bv = v; int bi = e;
; #pragma unroll
;             for (int o = 16; o >= 1; o >>= 1) { const float ov = __shfl_xor(bv, o); const int oi = __shfl_xor(bi, o); if (ov > bv || (ov == bv && oi < bi)) { bv = ov; bi = oi; } }
.LBB0_840:
	s_or_b64 exec, exec, s[4:5]
	v_or_b32_e32 v6, 16, v2
	v_lshl_add_u32 v2, v6, 7, v3
	ds_read_b32 v3, v2 offset:32768
	ds_bpermute_b32 v9, v145, v5
	s_waitcnt lgkmcnt(1)
	ds_bpermute_b32 v8, v145, v3
	s_waitcnt lgkmcnt(0)
	v_cmp_lt_f32_e64 s[8:9], v3, v8
	v_cmp_nlt_f32_e32 vcc, v3, v8
	s_and_saveexec_b64 s[10:11], vcc
	v_cmp_eq_f32_e32 vcc, v3, v8
	v_cmp_lt_i32_e64 s[4:5], v9, v5
	s_and_b64 s[4:5], vcc, s[4:5]
	s_andn2_b64 s[6:7], s[8:9], exec
	s_and_b64 s[4:5], s[4:5], exec
	s_or_b64 s[8:9], s[6:7], s[4:5]
	s_or_b64 exec, exec, s[10:11]
	v_mov_b32_e32 v4, v3
	v_mov_b32_e32 v2, v5
	v_mov_b32_e32 v7, v3
	s_and_saveexec_b64 s[4:5], s[8:9]
	v_mov_b32_e32 v4, v8
	v_mov_b32_e32 v2, v9
	v_mov_b32_e32 v7, v8
	s_or_b64 exec, exec, s[4:5]
	s_nop 1
	v_mov_b32_dpp v8, v4 row_ror:8 row_mask:0xf bank_mask:0xf
	s_nop 1
	v_mov_b32_dpp v9, v2 row_ror:8 row_mask:0xf bank_mask:0xf
	s_waitcnt lgkmcnt(1)
	v_cmp_lt_f32_e64 s[8:9], v7, v8
	v_cmp_nlt_f32_e32 vcc, v7, v8
	s_and_saveexec_b64 s[10:11], vcc
	s_cbranch_execz .LBB0_846
	v_cmp_eq_f32_e32 vcc, v7, v8
	s_waitcnt lgkmcnt(0)
	v_cmp_lt_i32_e64 s[4:5], v9, v2
	s_and_b64 s[4:5], vcc, s[4:5]
	s_andn2_b64 s[6:7], s[8:9], exec
	s_and_b64 s[4:5], s[4:5], exec
	s_or_b64 s[8:9], s[6:7], s[4:5]

; __device__ __forceinline__ void p6_router(Frame& F) {
;     ...
;             for (int o = 16; o >= 1; o >>= 1) { const float ov = __shfl_xor(bv, o); const int oi = __shfl_xor(bi, o); if (ov > bv || (ov == bv && oi < bi)) { bv = ov; bi = oi; } }
.LBB0_848:
	s_or_b64 exec, exec, s[4:5]
	s_nop 1
	v_mov_b32_dpp v8, v4 row_shl:4 row_mask:0xf bank_mask:0x5
	s_nop 1
	v_mov_b32_dpp v8, v4 row_shr:4 row_mask:0xf bank_mask:0xa
	s_waitcnt lgkmcnt(1)
	s_nop 1
	v_mov_b32_dpp v9, v2 row_shl:4 row_mask:0xf bank_mask:0x5
	s_nop 1
	v_mov_b32_dpp v9, v2 row_shr:4 row_mask:0xf bank_mask:0xa
	s_waitcnt lgkmcnt(1)
	v_cmp_lt_f32_e64 s[8:9], v7, v8
	v_cmp_nlt_f32_e32 vcc, v7, v8
	s_and_saveexec_b64 s[10:11], vcc
	s_cbranch_execz .LBB0_850
	v_cmp_eq_f32_e32 vcc, v7, v8
	s_waitcnt lgkmcnt(0)
	v_cmp_lt_i32_e64 s[4:5], v9, v2
	s_and_b64 s[4:5], vcc, s[4:5]
	s_andn2_b64 s[6:7], s[8:9], exec
	s_and_b64 s[4:5], s[4:5], exec
	s_or_b64 s[8:9], s[6:7], s[4:5]

; __device__ __forceinline__ void p6_router(Frame& F) {
;     ...
;             for (int o = 16; o >= 1; o >>= 1) { const float ov = __shfl_xor(bv, o); const int oi = __shfl_xor(bi, o); if (ov > bv || (ov == bv && oi < bi)) { bv = ov; bi = oi; } }
.LBB0_852:
	s_or_b64 exec, exec, s[4:5]
	s_nop 1
	v_mov_b32_dpp v8, v4 quad_perm:[2,3,0,1] row_mask:0xf bank_mask:0xf
	s_waitcnt lgkmcnt(1)
	s_nop 1
	v_mov_b32_dpp v9, v2 quad_perm:[2,3,0,1] row_mask:0xf bank_mask:0xf
	s_waitcnt lgkmcnt(1)
	v_cmp_lt_f32_e64 s[8:9], v7, v8
	v_cmp_nlt_f32_e32 vcc, v7, v8
	s_and_saveexec_b64 s[10:11], vcc
	s_cbranch_execz .LBB0_854
	v_cmp_eq_f32_e32 vcc, v7, v8
	s_waitcnt lgkmcnt(0)
	v_cmp_lt_i32_e64 s[4:5], v9, v2
	s_and_b64 s[4:5], vcc, s[4:5]
	s_andn2_b64 s[6:7], s[8:9], exec
	s_and_b64 s[4:5], s[4:5], exec
	s_or_b64 s[8:9], s[6:7], s[4:5]

; __device__ __forceinline__ void p6_router(Frame& F) {
;     ...
;             for (int o = 16; o >= 1; o >>= 1) { const float ov = __shfl_xor(bv, o); const int oi = __shfl_xor(bi, o); if (ov > bv || (ov == bv && oi < bi)) { bv = ov; bi = oi; } }
.LBB0_856:
	s_or_b64 exec, exec, s[4:5]
	s_nop 1
	v_mov_b32_dpp v4, v4 quad_perm:[1,0,3,2] row_mask:0xf bank_mask:0xf
	s_nop 1
	v_mov_b32_dpp v8, v2 quad_perm:[1,0,3,2] row_mask:0xf bank_mask:0xf
	s_waitcnt lgkmcnt(1)
	v_cmp_lt_f32_e64 s[8:9], v7, v4
	v_cmp_nlt_f32_e32 vcc, v7, v4
	s_and_saveexec_b64 s[10:11], vcc
	s_cbranch_execz .LBB0_858
	v_cmp_eq_f32_e32 vcc, v7, v4
	s_waitcnt lgkmcnt(0)
	v_cmp_lt_i32_e64 s[4:5], v8, v2
	s_and_b64 s[4:5], vcc, s[4:5]
	s_andn2_b64 s[6:7], s[8:9], exec
	s_and_b64 s[4:5], s[4:5], exec
	s_or_b64 s[8:9], s[6:7], s[4:5]

; __device__ __forceinline__ void p6_router(Frame& F) {
;     ...
;             float bv = v; int bi = e;
; #pragma unroll
;             for (int o = 16; o >= 1; o >>= 1) { const float ov = __shfl_xor(bv, o); const int oi = __shfl_xor(bi, o); if (ov > bv || (ov == bv && oi < bi)) { bv = ov; bi = oi; } }
;             tl[k] = bv; te[k] = bi; if (e == bi) v = -INFINITY;
.LBB0_860:
	s_or_b64 exec, exec, s[4:5]
	v_mov_b32_e32 v4, 0xff800000
	v_cmp_ne_u32_e32 vcc, v5, v2
	ds_bpermute_b32 v11, v145, v5
	s_nop 0
	v_cndmask_b32_e32 v4, v4, v3, vcc
	ds_bpermute_b32 v10, v145, v4
	s_waitcnt lgkmcnt(0)
	v_cmp_lt_f32_e64 s[8:9], v4, v10
	v_cmp_nlt_f32_e32 vcc, v4, v10
	s_and_saveexec_b64 s[10:11], vcc
	v_cmp_eq_f32_e32 vcc, v4, v10
	v_cmp_lt_i32_e64 s[4:5], v11, v5
	s_and_b64 s[4:5], vcc, s[4:5]
	s_andn2_b64 s[6:7], s[8:9], exec
	s_and_b64 s[4:5], s[4:5], exec
	s_or_b64 s[8:9], s[6:7], s[4:5]
	s_or_b64 exec, exec, s[10:11]
	v_mov_b32_e32 v9, v4
	v_mov_b32_e32 v3, v5
	v_mov_b32_e32 v8, v4
	s_and_saveexec_b64 s[4:5], s[8:9]
	v_mov_b32_e32 v9, v10
	v_mov_b32_e32 v3, v11
	v_mov_b32_e32 v8, v10
	s_or_b64 exec, exec, s[4:5]
	s_nop 1
	v_mov_b32_dpp v10, v9 row_ror:8 row_mask:0xf bank_mask:0xf
	s_nop 1
	v_mov_b32_dpp v11, v3 row_ror:8 row_mask:0xf bank_mask:0xf
	s_waitcnt lgkmcnt(1)
	v_cmp_lt_f32_e64 s[8:9], v8, v10
	v_cmp_nlt_f32_e32 vcc, v8, v10
	s_and_saveexec_b64 s[10:11], vcc
	s_cbranch_execz .LBB0_866
	v_cmp_eq_f32_e32 vcc, v8, v10
	s_waitcnt lgkmcnt(0)
	v_cmp_lt_i32_e64 s[4:5], v11, v3
	s_and_b64 s[4:5], vcc, s[4:5]
	s_andn2_b64 s[6:7], s[8:9], exec
	s_and_b64 s[4:5], s[4:5], exec
	s_or_b64 s[8:9], s[6:7], s[4:5]

; __device__ __forceinline__ void p6_router(Frame& F) {
;     ...
;             for (int o = 16; o >= 1; o >>= 1) { const float ov = __shfl_xor(bv, o); const int oi = __shfl_xor(bi, o); if (ov > bv || (ov == bv && oi < bi)) { bv = ov; bi = oi; } }
.LBB0_868:
	s_or_b64 exec, exec, s[4:5]
	s_nop 1
	v_mov_b32_dpp v10, v9 row_shl:4 row_mask:0xf bank_mask:0x5
	s_nop 1
	v_mov_b32_dpp v10, v9 row_shr:4 row_mask:0xf bank_mask:0xa
	s_waitcnt lgkmcnt(1)
	s_nop 1
	v_mov_b32_dpp v11, v3 row_shl:4 row_mask:0xf bank_mask:0x5
	s_nop 1
	v_mov_b32_dpp v11, v3 row_shr:4 row_mask:0xf bank_mask:0xa
	s_waitcnt lgkmcnt(1)
	v_cmp_lt_f32_e64 s[8:9], v8, v10
	v_cmp_nlt_f32_e32 vcc, v8, v10
	s_and_saveexec_b64 s[10:11], vcc
	s_cbranch_execz .LBB0_870
	v_cmp_eq_f32_e32 vcc, v8, v10
	s_waitcnt lgkmcnt(0)
	v_cmp_lt_i32_e64 s[4:5], v11, v3
	s_and_b64 s[4:5], vcc, s[4:5]
	s_andn2_b64 s[6:7], s[8:9], exec
	s_and_b64 s[4:5], s[4:5], exec
	s_or_b64 s[8:9], s[6:7], s[4:5]

; __device__ __forceinline__ void p6_router(Frame& F) {
;     ...
;             for (int o = 16; o >= 1; o >>= 1) { const float ov = __shfl_xor(bv, o); const int oi = __shfl_xor(bi, o); if (ov > bv || (ov == bv && oi < bi)) { bv = ov; bi = oi; } }
.LBB0_872:
	s_or_b64 exec, exec, s[4:5]
	s_nop 1
	v_mov_b32_dpp v10, v9 quad_perm:[2,3,0,1] row_mask:0xf bank_mask:0xf
	s_waitcnt lgkmcnt(1)
	s_nop 1
	v_mov_b32_dpp v11, v3 quad_perm:[2,3,0,1] row_mask:0xf bank_mask:0xf
	s_waitcnt lgkmcnt(1)
	v_cmp_lt_f32_e64 s[8:9], v8, v10
	v_cmp_nlt_f32_e32 vcc, v8, v10
	s_and_saveexec_b64 s[10:11], vcc
	s_cbranch_execz .LBB0_874
	v_cmp_eq_f32_e32 vcc, v8, v10
	s_waitcnt lgkmcnt(0)
	v_cmp_lt_i32_e64 s[4:5], v11, v3
	s_and_b64 s[4:5], vcc, s[4:5]
	s_andn2_b64 s[6:7], s[8:9], exec
	s_and_b64 s[4:5], s[4:5], exec
	s_or_b64 s[8:9], s[6:7], s[4:5]

; __device__ __forceinline__ void p6_router(Frame& F) {
;     ...
;             for (int o = 16; o >= 1; o >>= 1) { const float ov = __shfl_xor(bv, o); const int oi = __shfl_xor(bi, o); if (ov > bv || (ov == bv && oi < bi)) { bv = ov; bi = oi; } }
.LBB0_876:
	s_or_b64 exec, exec, s[4:5]
	s_nop 1
	v_mov_b32_dpp v9, v9 quad_perm:[1,0,3,2] row_mask:0xf bank_mask:0xf
	s_nop 1
	v_mov_b32_dpp v10, v3 quad_perm:[1,0,3,2] row_mask:0xf bank_mask:0xf
	s_waitcnt lgkmcnt(1)
	v_cmp_lt_f32_e64 s[8:9], v8, v9
	v_cmp_nlt_f32_e32 vcc, v8, v9
	s_and_saveexec_b64 s[10:11], vcc
	s_cbranch_execz .LBB0_878
	v_cmp_eq_f32_e32 vcc, v8, v9
	s_waitcnt lgkmcnt(0)
	v_cmp_lt_i32_e64 s[4:5], v10, v3
	s_and_b64 s[4:5], vcc, s[4:5]
	s_andn2_b64 s[6:7], s[8:9], exec
	s_and_b64 s[4:5], s[4:5], exec
	s_or_b64 s[8:9], s[6:7], s[4:5]

; __device__ __forceinline__ void p6_router(Frame& F) {
;     ...
;             float bv = v; int bi = e;
; #pragma unroll
;             for (int o = 16; o >= 1; o >>= 1) { const float ov = __shfl_xor(bv, o); const int oi = __shfl_xor(bi, o); if (ov > bv || (ov == bv && oi < bi)) { bv = ov; bi = oi; } }
;             tl[k] = bv; te[k] = bi; if (e == bi) v = -INFINITY;
.LBB0_880:
	s_or_b64 exec, exec, s[4:5]
	v_mov_b32_e32 v9, 0xff800000
	v_cmp_ne_u32_e32 vcc, v5, v3
	ds_bpermute_b32 v13, v145, v5
	s_waitcnt lgkmcnt(1)
	v_cndmask_b32_e32 v10, v9, v4, vcc
	ds_bpermute_b32 v12, v145, v10
	s_waitcnt lgkmcnt(0)
	v_cmp_lt_f32_e64 s[8:9], v10, v12
	v_cmp_nlt_f32_e32 vcc, v10, v12
	s_and_saveexec_b64 s[10:11], vcc
	v_cmp_eq_f32_e32 vcc, v10, v12
	v_cmp_lt_i32_e64 s[4:5], v13, v5
	s_and_b64 s[4:5], vcc, s[4:5]
	s_andn2_b64 s[6:7], s[8:9], exec
	s_and_b64 s[4:5], s[4:5], exec
	s_or_b64 s[8:9], s[6:7], s[4:5]
	s_or_b64 exec, exec, s[10:11]
	v_mov_b32_e32 v11, v10
	v_mov_b32_e32 v4, v5
	v_mov_b32_e32 v9, v10
	s_and_saveexec_b64 s[4:5], s[8:9]
	v_mov_b32_e32 v11, v12
	v_mov_b32_e32 v4, v13
	v_mov_b32_e32 v9, v12
	s_or_b64 exec, exec, s[4:5]
	s_nop 1
	v_mov_b32_dpp v12, v11 row_ror:8 row_mask:0xf bank_mask:0xf
	s_nop 1
	v_mov_b32_dpp v13, v4 row_ror:8 row_mask:0xf bank_mask:0xf
	s_waitcnt lgkmcnt(1)
	v_cmp_lt_f32_e64 s[8:9], v9, v12
	v_cmp_nlt_f32_e32 vcc, v9, v12
	s_and_saveexec_b64 s[10:11], vcc
	s_cbranch_execz .LBB0_886
	v_cmp_eq_f32_e32 vcc, v9, v12
	s_waitcnt lgkmcnt(0)
	v_cmp_lt_i32_e64 s[4:5], v13, v4
	s_and_b64 s[4:5], vcc, s[4:5]
	s_andn2_b64 s[6:7], s[8:9], exec
	s_and_b64 s[4:5], s[4:5], exec
	s_or_b64 s[8:9], s[6:7], s[4:5]

; __device__ __forceinline__ void p6_router(Frame& F) {
;     ...
;             for (int o = 16; o >= 1; o >>= 1) { const float ov = __shfl_xor(bv, o); const int oi = __shfl_xor(bi, o); if (ov > bv || (ov == bv && oi < bi)) { bv = ov; bi = oi; } }
.LBB0_888:
	s_or_b64 exec, exec, s[4:5]
	s_nop 1
	v_mov_b32_dpp v12, v11 row_shl:4 row_mask:0xf bank_mask:0x5
	s_nop 1
	v_mov_b32_dpp v12, v11 row_shr:4 row_mask:0xf bank_mask:0xa
	s_waitcnt lgkmcnt(1)
	s_nop 1
	v_mov_b32_dpp v13, v4 row_shl:4 row_mask:0xf bank_mask:0x5
	s_nop 1
	v_mov_b32_dpp v13, v4 row_shr:4 row_mask:0xf bank_mask:0xa
	s_waitcnt lgkmcnt(1)
	v_cmp_lt_f32_e64 s[8:9], v9, v12
	v_cmp_nlt_f32_e32 vcc, v9, v12
	s_and_saveexec_b64 s[10:11], vcc
	s_cbranch_execz .LBB0_890
	v_cmp_eq_f32_e32 vcc, v9, v12
	s_waitcnt lgkmcnt(0)
	v_cmp_lt_i32_e64 s[4:5], v13, v4
	s_and_b64 s[4:5], vcc, s[4:5]
	s_andn2_b64 s[6:7], s[8:9], exec
	s_and_b64 s[4:5], s[4:5], exec
	s_or_b64 s[8:9], s[6:7], s[4:5]

; __device__ __forceinline__ void p6_router(Frame& F) {
;     ...
;             for (int o = 16; o >= 1; o >>= 1) { const float ov = __shfl_xor(bv, o); const int oi = __shfl_xor(bi, o); if (ov > bv || (ov == bv && oi < bi)) { bv = ov; bi = oi; } }
.LBB0_892:
	s_or_b64 exec, exec, s[4:5]
	s_nop 1
	v_mov_b32_dpp v12, v11 quad_perm:[2,3,0,1] row_mask:0xf bank_mask:0xf
	s_waitcnt lgkmcnt(1)
	s_nop 1
	v_mov_b32_dpp v13, v4 quad_perm:[2,3,0,1] row_mask:0xf bank_mask:0xf
	s_waitcnt lgkmcnt(1)
	v_cmp_lt_f32_e64 s[8:9], v9, v12
	v_cmp_nlt_f32_e32 vcc, v9, v12
	s_and_saveexec_b64 s[10:11], vcc
	s_cbranch_execz .LBB0_894
	v_cmp_eq_f32_e32 vcc, v9, v12
	s_waitcnt lgkmcnt(0)
	v_cmp_lt_i32_e64 s[4:5], v13, v4
	s_and_b64 s[4:5], vcc, s[4:5]
	s_andn2_b64 s[6:7], s[8:9], exec
	s_and_b64 s[4:5], s[4:5], exec
	s_or_b64 s[8:9], s[6:7], s[4:5]

; __device__ __forceinline__ void p6_router(Frame& F) {
;     ...
;             for (int o = 16; o >= 1; o >>= 1) { const float ov = __shfl_xor(bv, o); const int oi = __shfl_xor(bi, o); if (ov > bv || (ov == bv && oi < bi)) { bv = ov; bi = oi; } }
.LBB0_896:
	s_or_b64 exec, exec, s[4:5]
	s_nop 1
	v_mov_b32_dpp v11, v11 quad_perm:[1,0,3,2] row_mask:0xf bank_mask:0xf
	s_nop 1
	v_mov_b32_dpp v12, v4 quad_perm:[1,0,3,2] row_mask:0xf bank_mask:0xf
	s_waitcnt lgkmcnt(1)
	v_cmp_lt_f32_e64 s[8:9], v9, v11
	v_cmp_nlt_f32_e32 vcc, v9, v11
	s_and_saveexec_b64 s[10:11], vcc
	s_cbranch_execz .LBB0_898
	v_cmp_eq_f32_e32 vcc, v9, v11
	s_waitcnt lgkmcnt(0)
	v_cmp_lt_i32_e64 s[4:5], v12, v4
	s_and_b64 s[4:5], vcc, s[4:5]
	s_andn2_b64 s[6:7], s[8:9], exec
	s_and_b64 s[4:5], s[4:5], exec
	s_or_b64 s[8:9], s[6:7], s[4:5]

; __device__ __forceinline__ void p6_router(Frame& F) {
;     ...
;             float bv = v; int bi = e;
; #pragma unroll
;             for (int o = 16; o >= 1; o >>= 1) { const float ov = __shfl_xor(bv, o); const int oi = __shfl_xor(bi, o); if (ov > bv || (ov == bv && oi < bi)) { bv = ov; bi = oi; } }
;             tl[k] = bv; te[k] = bi; if (e == bi) v = -INFINITY;
.LBB0_900:
	s_or_b64 exec, exec, s[4:5]
	v_mov_b32_e32 v11, 0xff800000
	v_cmp_ne_u32_e32 vcc, v5, v4
	s_waitcnt lgkmcnt(0)
	ds_bpermute_b32 v12, v145, v5
	v_cndmask_b32_e32 v10, v11, v10, vcc
	ds_bpermute_b32 v11, v145, v10
	s_waitcnt lgkmcnt(0)
	v_cmp_lt_f32_e64 s[8:9], v10, v11
	v_cmp_nlt_f32_e32 vcc, v10, v11
	s_and_saveexec_b64 s[10:11], vcc
	v_cmp_eq_f32_e32 vcc, v10, v11
	v_cmp_lt_i32_e64 s[4:5], v12, v5
	s_and_b64 s[4:5], vcc, s[4:5]
	s_andn2_b64 s[6:7], s[8:9], exec
	s_and_b64 s[4:5], s[4:5], exec
	s_or_b64 s[8:9], s[6:7], s[4:5]
	s_or_b64 exec, exec, s[10:11]
	s_and_saveexec_b64 s[4:5], s[8:9]
	v_mov_b32_e32 v10, v11
	v_mov_b32_e32 v5, v12
	s_or_b64 exec, exec, s[4:5]
	s_nop 1
	v_mov_b32_dpp v11, v10 row_ror:8 row_mask:0xf bank_mask:0xf
	s_nop 1
	v_mov_b32_dpp v12, v5 row_ror:8 row_mask:0xf bank_mask:0xf
	s_waitcnt lgkmcnt(1)
	v_cmp_lt_f32_e64 s[8:9], v10, v11
	v_cmp_nlt_f32_e32 vcc, v10, v11
	s_and_saveexec_b64 s[10:11], vcc
	s_cbranch_execz .LBB0_906
	v_cmp_eq_f32_e32 vcc, v10, v11
	s_waitcnt lgkmcnt(0)
	v_cmp_lt_i32_e64 s[4:5], v12, v5
	s_and_b64 s[4:5], vcc, s[4:5]
	s_andn2_b64 s[6:7], s[8:9], exec
	s_and_b64 s[4:5], s[4:5], exec
	s_or_b64 s[8:9], s[6:7], s[4:5]

; __device__ __forceinline__ void p6_router(Frame& F) {
;     ...
;             for (int o = 16; o >= 1; o >>= 1) { const float ov = __shfl_xor(bv, o); const int oi = __shfl_xor(bi, o); if (ov > bv || (ov == bv && oi < bi)) { bv = ov; bi = oi; } }
.LBB0_908:
	s_or_b64 exec, exec, s[4:5]
	s_nop 1
	v_mov_b32_dpp v11, v10 row_shl:4 row_mask:0xf bank_mask:0x5
	s_nop 1
	v_mov_b32_dpp v11, v10 row_shr:4 row_mask:0xf bank_mask:0xa
	s_waitcnt lgkmcnt(1)
	s_nop 1
	v_mov_b32_dpp v12, v5 row_shl:4 row_mask:0xf bank_mask:0x5
	s_nop 1
	v_mov_b32_dpp v12, v5 row_shr:4 row_mask:0xf bank_mask:0xa
	s_waitcnt lgkmcnt(1)
	v_cmp_lt_f32_e64 s[8:9], v10, v11
	v_cmp_nlt_f32_e32 vcc, v10, v11
	s_and_saveexec_b64 s[10:11], vcc
	s_cbranch_execz .LBB0_910
	v_cmp_eq_f32_e32 vcc, v10, v11
	s_waitcnt lgkmcnt(0)
	v_cmp_lt_i32_e64 s[4:5], v12, v5
	s_and_b64 s[4:5], vcc, s[4:5]
	s_andn2_b64 s[6:7], s[8:9], exec
	s_and_b64 s[4:5], s[4:5], exec
	s_or_b64 s[8:9], s[6:7], s[4:5]

; __device__ __forceinline__ void p6_router(Frame& F) {
;     ...
;             for (int o = 16; o >= 1; o >>= 1) { const float ov = __shfl_xor(bv, o); const int oi = __shfl_xor(bi, o); if (ov > bv || (ov == bv && oi < bi)) { bv = ov; bi = oi; } }
.LBB0_912:
	s_or_b64 exec, exec, s[4:5]
	s_nop 1
	v_mov_b32_dpp v11, v10 quad_perm:[2,3,0,1] row_mask:0xf bank_mask:0xf
	s_waitcnt lgkmcnt(1)
	s_nop 1
	v_mov_b32_dpp v12, v5 quad_perm:[2,3,0,1] row_mask:0xf bank_mask:0xf
	s_waitcnt lgkmcnt(1)
	v_cmp_lt_f32_e64 s[8:9], v10, v11
	v_cmp_nlt_f32_e32 vcc, v10, v11
	s_and_saveexec_b64 s[10:11], vcc
	s_cbranch_execz .LBB0_914
	v_cmp_eq_f32_e32 vcc, v10, v11
	s_waitcnt lgkmcnt(0)
	v_cmp_lt_i32_e64 s[4:5], v12, v5
	s_and_b64 s[4:5], vcc, s[4:5]
	s_andn2_b64 s[6:7], s[8:9], exec
	s_and_b64 s[4:5], s[4:5], exec
	s_or_b64 s[8:9], s[6:7], s[4:5]

; __device__ __forceinline__ void p6_router(Frame& F) {
;     ...
;             for (int o = 16; o >= 1; o >>= 1) { const float ov = __shfl_xor(bv, o); const int oi = __shfl_xor(bi, o); if (ov > bv || (ov == bv && oi < bi)) { bv = ov; bi = oi; } }
;             tl[k] = bv; te[k] = bi; if (e == bi) v = -INFINITY;
.LBB0_916:
	s_or_b64 exec, exec, s[4:5]
	s_nop 1
	v_mov_b32_dpp v11, v10 quad_perm:[1,0,3,2] row_mask:0xf bank_mask:0xf
	s_nop 1
	v_mov_b32_dpp v1, v5 quad_perm:[1,0,3,2] row_mask:0xf bank_mask:0xf
	s_waitcnt lgkmcnt(1)
	v_cmp_lt_f32_e64 s[8:9], v10, v11
	v_cmp_nlt_f32_e32 vcc, v10, v11
	s_and_saveexec_b64 s[10:11], vcc
	s_cbranch_execz .LBB0_945
	v_cmp_eq_f32_e32 vcc, v10, v11
	s_waitcnt lgkmcnt(0)
	v_cmp_lt_i32_e64 s[4:5], v1, v5
	s_and_b64 s[4:5], vcc, s[4:5]
	s_andn2_b64 s[6:7], s[8:9], exec
	s_and_b64 s[4:5], s[4:5], exec
	s_or_b64 s[8:9], s[6:7], s[4:5]
	s_or_b64 exec, exec, s[10:11]
	s_and_saveexec_b64 s[4:5], s[8:9]
	s_cbranch_execnz .LBB0_946
